# baseline (speedup 1.0000x reference)
.LBB0_6:
	s_or_b64 exec, exec, s[6:7]
	s_load_dwordx2 s[10:11], s[0:1], 0x30
	v_and_b32_e32 v1, 15, v0
	v_bfe_u32 v2, v0, 4, 2
	v_lshrrev_b32_e32 v3, 6, v0
	s_movk_i32 s8, 0x90
	s_movk_i32 s9, 0x1b0
	v_mul_u32_u24_e32 v4, 0x900, v3
	v_mad_u32_u24 v4, v1, s8, v4
	v_mad_u32_u24 v4, v2, 36, v4
	v_lshlrev_b32_e32 v5, 2, v1
	v_mad_u32_u24 v5, v2, s9, v5
	v_add_u32_e32 v5, 0x2400, v5
	s_waitcnt lgkmcnt(0)
	s_barrier
	ds_read_b32 v10, v4
	ds_read_b32 v11, v4 offset:4
	ds_read_b32 v12, v4 offset:8
	ds_read_b32 v13, v4 offset:12
	ds_read_b32 v14, v4 offset:16
	ds_read_b32 v15, v4 offset:20
	ds_read_b32 v16, v4 offset:24
	ds_read_b32 v17, v4 offset:28
	ds_read_b32 v18, v4 offset:32
	ds_read_b32 v20, v5
	ds_read_b32 v21, v5 offset:72
	ds_read_b32 v22, v5 offset:144
	ds_read_b32 v23, v5 offset:216
	s_waitcnt lgkmcnt(0)
	ds_read_b32 v24, v5 offset:4
	ds_read_b32 v25, v5 offset:76
	ds_read_b32 v26, v5 offset:148
	ds_read_b32 v27, v5 offset:220
	ds_read_b32 v28, v5 offset:8
	ds_read_b32 v29, v5 offset:80
	ds_read_b32 v30, v5 offset:152
	ds_read_b32 v31, v5 offset:224
	v_mfma_f32_16x16x4_f32 v[60:63], v10, v20, 0
	v_mfma_f32_16x16x4_f32 v[64:67], v10, v21, 0
	v_mfma_f32_16x16x4_f32 v[68:71], v10, v22, 0
	v_mfma_f32_16x16x4_f32 v[72:75], v10, v23, 0
	s_waitcnt lgkmcnt(4)
	ds_read_b32 v32, v5 offset:72
	ds_read_b32 v33, v5 offset:144
	ds_read_b32 v34, v5 offset:216
	ds_read_b32 v35, v5 offset:288
	v_mfma_f32_16x16x4_f32 v[60:63], v11, v24, v[60:63]
	v_mfma_f32_16x16x4_f32 v[64:67], v11, v25, v[64:67]
	v_mfma_f32_16x16x4_f32 v[68:71], v11, v26, v[68:71]
	v_mfma_f32_16x16x4_f32 v[72:75], v11, v27, v[72:75]
	s_waitcnt lgkmcnt(4)
	ds_read_b32 v36, v5 offset:76
	ds_read_b32 v37, v5 offset:148
	ds_read_b32 v38, v5 offset:220
	ds_read_b32 v39, v5 offset:292
	v_mfma_f32_16x16x4_f32 v[60:63], v12, v28, v[60:63]
	v_mfma_f32_16x16x4_f32 v[64:67], v12, v29, v[64:67]
	v_mfma_f32_16x16x4_f32 v[68:71], v12, v30, v[68:71]
	v_mfma_f32_16x16x4_f32 v[72:75], v12, v31, v[72:75]
	s_waitcnt lgkmcnt(4)
	ds_read_b32 v40, v5 offset:80
	ds_read_b32 v41, v5 offset:152
	ds_read_b32 v42, v5 offset:224
	ds_read_b32 v43, v5 offset:296
	v_mfma_f32_16x16x4_f32 v[60:63], v13, v32, v[60:63]
	v_mfma_f32_16x16x4_f32 v[64:67], v13, v33, v[64:67]
	v_mfma_f32_16x16x4_f32 v[68:71], v13, v34, v[68:71]
	v_mfma_f32_16x16x4_f32 v[72:75], v13, v35, v[72:75]
	s_waitcnt lgkmcnt(4)
	ds_read_b32 v44, v5 offset:144
	ds_read_b32 v45, v5 offset:216
	ds_read_b32 v46, v5 offset:288
	ds_read_b32 v47, v5 offset:360
	v_mfma_f32_16x16x4_f32 v[60:63], v14, v36, v[60:63]
	v_mfma_f32_16x16x4_f32 v[64:67], v14, v37, v[64:67]
	v_mfma_f32_16x16x4_f32 v[68:71], v14, v38, v[68:71]
	v_mfma_f32_16x16x4_f32 v[72:75], v14, v39, v[72:75]
	s_waitcnt lgkmcnt(4)
	ds_read_b32 v48, v5 offset:148
	ds_read_b32 v49, v5 offset:220
	ds_read_b32 v50, v5 offset:292
	ds_read_b32 v51, v5 offset:364
	v_mfma_f32_16x16x4_f32 v[60:63], v15, v40, v[60:63]
	v_mfma_f32_16x16x4_f32 v[64:67], v15, v41, v[64:67]
	v_mfma_f32_16x16x4_f32 v[68:71], v15, v42, v[68:71]
	v_mfma_f32_16x16x4_f32 v[72:75], v15, v43, v[72:75]
	s_waitcnt lgkmcnt(4)
	ds_read_b32 v52, v5 offset:152
	ds_read_b32 v53, v5 offset:224
	ds_read_b32 v54, v5 offset:296
	ds_read_b32 v55, v5 offset:368
	v_mfma_f32_16x16x4_f32 v[60:63], v16, v44, v[60:63]
	v_mfma_f32_16x16x4_f32 v[64:67], v16, v45, v[64:67]
	v_mfma_f32_16x16x4_f32 v[68:71], v16, v46, v[68:71]
	v_mfma_f32_16x16x4_f32 v[72:75], v16, v47, v[72:75]
	s_waitcnt lgkmcnt(4)
	v_mfma_f32_16x16x4_f32 v[60:63], v17, v48, v[60:63]
	v_mfma_f32_16x16x4_f32 v[64:67], v17, v49, v[64:67]
	v_mfma_f32_16x16x4_f32 v[68:71], v17, v50, v[68:71]
	v_mfma_f32_16x16x4_f32 v[72:75], v17, v51, v[72:75]
	s_waitcnt lgkmcnt(0)
	v_mfma_f32_16x16x4_f32 v[60:63], v18, v52, v[60:63]
	v_mfma_f32_16x16x4_f32 v[64:67], v18, v53, v[64:67]
	v_mfma_f32_16x16x4_f32 v[68:71], v18, v54, v[68:71]
	v_mfma_f32_16x16x4_f32 v[72:75], v18, v55, v[72:75]
	s_lshl_b32 s8, s12, 7
	s_add_i32 s8, s8, s3
	v_add_u32_e32 v6, s8, v1
	v_lshlrev_b32_e32 v6, 7, v6
	v_lshl_add_u32 v6, v3, 5, v6
	v_lshl_add_u32 v6, v2, 3, v6
	v_add_u32_e32 v7, 0x4000, v6
	v_add_u32_e32 v8, 0x8000, v6
	v_add_u32_e32 v9, 0xc000, v6
	v_and_b32_e32 v94, 63, v0
	v_lshlrev_b32_e32 v95, 3, v3
	s_nop 7
	s_nop 7
	v_cvt_pk_f16_f32 v80, v60, v61
	v_cvt_pk_f16_f32 v81, v62, v63
	v_cvt_pk_f16_f32 v82, v64, v65
	v_cvt_pk_f16_f32 v83, v66, v67
	v_cvt_pk_f16_f32 v84, v68, v69
	v_cvt_pk_f16_f32 v85, v70, v71
	v_cvt_pk_f16_f32 v86, v72, v73
	v_cvt_pk_f16_f32 v87, v74, v75
	s_waitcnt lgkmcnt(0)
	global_store_dwordx2 v6, v[80:81], s[10:11]
	global_store_dwordx2 v7, v[82:83], s[10:11]
	global_store_dwordx2 v8, v[84:85], s[10:11]
	global_store_dwordx2 v9, v[86:87], s[10:11]
	v_add_f32_e32 v90, v60, v61
	v_mul_f32_e32 v91, v60, v60
	v_fmac_f32_e32 v91, v61, v61
	v_add_f32_e32 v90, v90, v62
	v_fmac_f32_e32 v91, v62, v62
	v_add_f32_e32 v90, v90, v63
	v_fmac_f32_e32 v91, v63, v63
	v_add_f32_e32 v90, v90, v64
	v_fmac_f32_e32 v91, v64, v64
	v_add_f32_e32 v90, v90, v65
	v_fmac_f32_e32 v91, v65, v65
	v_add_f32_e32 v90, v90, v66
	v_fmac_f32_e32 v91, v66, v66
	v_add_f32_e32 v90, v90, v67
	v_fmac_f32_e32 v91, v67, v67
	v_add_f32_e32 v90, v90, v68
	v_fmac_f32_e32 v91, v68, v68
	v_add_f32_e32 v90, v90, v69
	v_fmac_f32_e32 v91, v69, v69
	v_add_f32_e32 v90, v90, v70
	v_fmac_f32_e32 v91, v70, v70
	v_add_f32_e32 v90, v90, v71
	v_fmac_f32_e32 v91, v71, v71
	v_add_f32_e32 v90, v90, v72
	v_fmac_f32_e32 v91, v72, v72
	v_add_f32_e32 v90, v90, v73
	v_fmac_f32_e32 v91, v73, v73
	v_add_f32_e32 v90, v90, v74
	v_fmac_f32_e32 v91, v74, v74
	v_add_f32_e32 v90, v90, v75
	v_fmac_f32_e32 v91, v75, v75
	v_mov_b32_e32 v96, 0
	v_mov_b32_e32 v97, 0
	v_cmp_eq_u32_e32 vcc, 63, v94
	s_nop 1
	v_mov_b32_dpp v92, v90 row_shr:1 row_mask:0xf bank_mask:0xf bound_ctrl:1
	v_mov_b32_dpp v93, v91 row_shr:1 row_mask:0xf bank_mask:0xf bound_ctrl:1
	v_pk_add_f32 v[90:91], v[90:91], v[92:93]
	s_nop 1
	v_mov_b32_dpp v92, v90 row_shr:2 row_mask:0xf bank_mask:0xf bound_ctrl:1
	v_mov_b32_dpp v93, v91 row_shr:2 row_mask:0xf bank_mask:0xf bound_ctrl:1
	v_pk_add_f32 v[90:91], v[90:91], v[92:93]
	s_nop 1
	v_mov_b32_dpp v92, v90 row_shr:4 row_mask:0xf bank_mask:0xf bound_ctrl:1
	v_mov_b32_dpp v93, v91 row_shr:4 row_mask:0xf bank_mask:0xf bound_ctrl:1
	v_pk_add_f32 v[90:91], v[90:91], v[92:93]
	s_nop 1
	v_mov_b32_dpp v92, v90 row_shr:8 row_mask:0xf bank_mask:0xf bound_ctrl:1
	v_mov_b32_dpp v93, v91 row_shr:8 row_mask:0xf bank_mask:0xf bound_ctrl:1
	v_pk_add_f32 v[90:91], v[90:91], v[92:93]
	v_mov_b32_e32 v92, 0
	v_mov_b32_e32 v93, 0
	s_nop 0
	v_mov_b32_dpp v92, v90 row_bcast:15 row_mask:0xa bank_mask:0xf
	v_mov_b32_dpp v93, v91 row_bcast:15 row_mask:0xa bank_mask:0xf
	v_pk_add_f32 v[90:91], v[90:91], v[92:93]
	s_nop 1
	v_mov_b32_dpp v96, v90 row_bcast:31 row_mask:0xc bank_mask:0xf
	v_mov_b32_dpp v97, v91 row_bcast:31 row_mask:0xc bank_mask:0xf
	s_and_saveexec_b64 s[6:7], vcc
	v_pk_add_f32 v[90:91], v[90:91], v[96:97]
	s_lshl_b32 s8, s2, 5
	s_add_i32 s8, s8, 0xda000
	v_add_u32_e32 v95, s8, v95
	global_store_dwordx2 v95, v[90:91], s[4:5]
	s_or_b64 exec, exec, s[6:7]

_Z4khidPKDF16_PKfS2_S2_S0_PDF16_Pf:
	s_load_dwordx8 s[4:11], s[0:1], 0x0
	s_load_dwordx2 s[12:13], s[0:1], 0x20
	s_load_dwordx2 s[22:23], s[0:1], 0x30
	s_load_dwordx2 s[24:25], s[0:1], 0x28
	v_lshlrev_b32_e32 v1, 3, v0
	s_lshr_b32 s3, s2, 1
	v_and_b32_e32 v2, 56, v1
	s_and_b32 s15, s3, 0x7ffffffc
	s_lshl_b32 s14, s2, 4
	v_lshlrev_b32_e32 v106, 1, v2
	v_mov_b32_e32 v107, 0
	s_and_b32 s14, s14, 0x70
	v_lshlrev_b32_e32 v126, 2, v2
	s_add_i32 s16, s15, -1
	s_waitcnt lgkmcnt(0)
	s_sub_u32 s26, s24, s4
	s_subb_u32 s27, s25, s5
	s_cmp_eq_u32 s27, 0
	s_cselect_b32 s28, s4, s24
	s_cselect_b32 s29, s5, s25
	s_sub_u32 s28, s28, 0x100000
	s_subb_u32 s29, s29, 0
	s_sub_u32 s30, s6, s28
	s_lshl_b32 s30, s30, 2
	s_add_u32 s30, s30, 0xda000
	s_add_u32 s30, s28, s30
	s_addc_u32 s31, s29, 0
	s_sub_u32 s32, s22, s28
	s_lshl_b32 s33, s32, 2
	s_add_u32 s33, s33, 0xda000
	s_add_u32 s34, s28, s33
	s_addc_u32 s35, s29, 0
	v_and_b32_e32 v132, 63, v0
	v_lshlrev_b32_e32 v132, 4, v132
	v_add_u32_e32 v133, 0x1000, v132
	global_load_dwordx4 v[134:137], v132, s[30:31]
	global_load_dwordx4 v[138:141], v132, s[30:31] offset:1024
	global_load_dwordx4 v[142:145], v132, s[30:31] offset:2048
	global_load_dwordx4 v[146:149], v132, s[30:31] offset:3072
	global_load_dwordx4 v[150:153], v133, s[30:31]
	global_load_dwordx4 v[154:157], v133, s[30:31] offset:1024
	global_load_dwordx4 v[158:161], v133, s[30:31] offset:2048
	global_load_dwordx4 v[162:165], v133, s[30:31] offset:3072
	v_lshl_add_u64 v[2:3], s[4:5], 0, v[106:107]
	v_mul_u32_u24_e32 v1, 0x1c8, v0
	s_movk_i32 s4, 0xffee
	v_lshrrev_b32_e32 v114, 3, v0
	s_add_i32 s17, s14, -1
	v_mul_i32_i24_sdwa v4, v1, s4 dst_sel:DWORD dst_unused:UNUSED_PAD src0_sel:WORD_1 src1_sel:DWORD
	v_add_u32_sdwa v124, s16, v1 dst_sel:DWORD dst_unused:UNUSED_PAD src0_sel:DWORD src1_sel:WORD_1
	s_movk_i32 s4, 0x7f
	v_add3_u32 v125, s17, v114, v4
	v_med3_i32 v1, v124, 0, s4
	v_med3_i32 v4, v125, 0, s4
	v_lshlrev_b32_e32 v1, 14, v1
	v_or_b32_e32 v121, 32, v114
	v_lshl_or_b32 v106, v4, 7, v1
	v_mul_lo_u16_e32 v1, 57, v121
	v_lshrrev_b16_e32 v1, 10, v1
	v_mul_i32_i24_e32 v6, 0xffffffee, v1
	v_add_u32_e32 v122, s16, v1
	v_add3_u32 v123, s17, v121, v6
	v_min_u32_e32 v1, 0x7f, v122
	v_med3_i32 v6, v123, 0, s4
	v_lshlrev_b32_e32 v1, 14, v1
	v_or_b32_e32 v118, 64, v114
	v_lshl_add_u64 v[4:5], v[2:3], 0, v[106:107]
	v_lshl_or_b32 v106, v6, 7, v1
	v_mul_lo_u16_e32 v1, 57, v118
	v_lshrrev_b16_e32 v1, 10, v1
	v_lshl_add_u64 v[6:7], v[2:3], 0, v[106:107]
	global_load_dwordx4 v[86:89], v[4:5], off
	global_load_dwordx4 v[82:85], v[6:7], off
	v_mul_i32_i24_e32 v4, 0xffffffee, v1
	v_add_u32_e32 v119, s16, v1
	v_add3_u32 v120, s17, v118, v4
	v_min_u32_e32 v1, 0x7f, v119
	v_med3_i32 v4, v120, 0, s4
	v_lshlrev_b32_e32 v1, 14, v1
	v_or_b32_e32 v115, 0x60, v114
	v_lshl_or_b32 v106, v4, 7, v1
	v_mul_lo_u16_e32 v1, 57, v115
	v_lshrrev_b16_e32 v1, 10, v1
	v_mul_i32_i24_e32 v6, 0xffffffee, v1
	v_add_u32_e32 v116, s16, v1
	v_add3_u32 v117, s17, v115, v6
	v_min_u32_e32 v1, 0x7f, v116
	v_med3_i32 v6, v117, 0, s4
	v_lshlrev_b32_e32 v1, 14, v1
	v_lshrrev_b32_e32 v112, 6, v0
	v_lshl_add_u64 v[4:5], v[2:3], 0, v[106:107]
	v_lshl_or_b32 v106, v6, 7, v1
	v_mul_u32_u24_e32 v1, 0x480, v112
	v_and_b32_e32 v113, 63, v0
	v_lshl_add_u64 v[2:3], v[2:3], 0, v[106:107]
	v_lshlrev_b32_e32 v106, 4, v1
	global_load_dwordx4 v[78:81], v[4:5], off
	global_load_dwordx4 v[74:77], v[2:3], off
	v_lshl_add_u64 v[2:3], s[12:13], 0, v[106:107]
	v_lshlrev_b32_e32 v106, 4, v113
	v_lshl_add_u64 v[2:3], v[2:3], 0, v[106:107]
	s_movk_i32 s4, 0x1000
	v_add_co_u32_e32 v4, vcc, s4, v2
	s_movk_i32 s4, 0x2000
	s_nop 0
	v_addc_co_u32_e32 v5, vcc, 0, v3, vcc
	v_add_co_u32_e32 v90, vcc, s4, v2
	s_movk_i32 s4, 0x3000
	s_nop 0
	v_addc_co_u32_e32 v91, vcc, 0, v3, vcc
	v_add_co_u32_e32 v92, vcc, s4, v2
	s_movk_i32 s4, 0x4000
	s_nop 0
	v_addc_co_u32_e32 v93, vcc, 0, v3, vcc
	v_add_co_u32_e32 v110, vcc, s4, v2
	global_load_dwordx4 v[70:73], v[2:3], off
	global_load_dwordx4 v[66:69], v[2:3], off offset:1024
	v_addc_co_u32_e32 v111, vcc, 0, v3, vcc
	global_load_dwordx4 v[62:65], v[2:3], off offset:2048
	global_load_dwordx4 v[58:61], v[2:3], off offset:3072
	global_load_dwordx4 v[50:53], v[4:5], off offset:1024
	global_load_dwordx4 v[46:49], v[4:5], off offset:2048
	global_load_dwordx4 v[42:45], v[4:5], off offset:3072
	global_load_dwordx4 v[18:21], v[92:93], off offset:1024
	global_load_dwordx4 v[14:17], v[92:93], off offset:2048
	global_load_dwordx4 v[10:13], v[92:93], off offset:3072
	global_load_dwordx4 v[54:57], v[90:91], off offset:-4096
	global_load_dwordx4 v[38:41], v[90:91], off
	global_load_dwordx4 v[34:37], v[90:91], off offset:1024
	global_load_dwordx4 v[30:33], v[90:91], off offset:2048
	global_load_dwordx4 v[26:29], v[90:91], off offset:3072
	global_load_dwordx4 v[22:25], v[110:111], off offset:-4096
	global_load_dwordx4 v[6:9], v[110:111], off
	s_nop 0
	global_load_dwordx4 v[2:5], v[110:111], off offset:1024
	global_load_dwordx4 v[94:97], v126, s[8:9] offset:16
	global_load_dwordx4 v[90:93], v126, s[10:11] offset:16
	global_load_dwordx4 v[102:105], v126, s[8:9]
	global_load_dwordx4 v[98:101], v126, s[10:11]
	v_cmp_eq_u32_e64 s[4:5], 63, v113
	s_waitcnt vmcnt(26)
	v_pk_add_f32 v[134:135], v[134:135], v[136:137]
	v_pk_add_f32 v[138:139], v[138:139], v[140:141]
	v_pk_add_f32 v[142:143], v[142:143], v[144:145]
	v_pk_add_f32 v[146:147], v[146:147], v[148:149]
	v_pk_add_f32 v[150:151], v[150:151], v[152:153]
	v_pk_add_f32 v[154:155], v[154:155], v[156:157]
	v_pk_add_f32 v[158:159], v[158:159], v[160:161]
	v_pk_add_f32 v[162:163], v[162:163], v[164:165]
	v_pk_add_f32 v[134:135], v[134:135], v[138:139]
	v_pk_add_f32 v[142:143], v[142:143], v[146:147]
	v_pk_add_f32 v[150:151], v[150:151], v[154:155]
	v_pk_add_f32 v[158:159], v[158:159], v[162:163]
	v_pk_add_f32 v[134:135], v[134:135], v[142:143]
	v_pk_add_f32 v[150:151], v[150:151], v[158:159]
	v_pk_add_f32 v[108:109], v[134:135], v[150:151]
	s_nop 1
	v_mov_b32_dpp v110, v108 row_shr:1 row_mask:0xf bank_mask:0xf bound_ctrl:1
	v_mov_b32_dpp v111, v109 row_shr:1 row_mask:0xf bank_mask:0xf bound_ctrl:1
	v_pk_add_f32 v[108:109], v[108:109], v[110:111]
	v_lshlrev_b32_e32 v1, 3, v112
	s_nop 0
	v_mov_b32_dpp v110, v108 row_shr:2 row_mask:0xf bank_mask:0xf bound_ctrl:1
	v_mov_b32_dpp v111, v109 row_shr:2 row_mask:0xf bank_mask:0xf bound_ctrl:1
	v_pk_add_f32 v[108:109], v[108:109], v[110:111]
	s_nop 1
	v_mov_b32_dpp v110, v108 row_shr:4 row_mask:0xf bank_mask:0xf bound_ctrl:1
	v_mov_b32_dpp v111, v109 row_shr:4 row_mask:0xf bank_mask:0xf bound_ctrl:1
	v_pk_add_f32 v[108:109], v[108:109], v[110:111]
	s_nop 1
	v_mov_b32_dpp v110, v108 row_shr:8 row_mask:0xf bank_mask:0xf bound_ctrl:1
	v_mov_b32_dpp v111, v109 row_shr:8 row_mask:0xf bank_mask:0xf bound_ctrl:1
	v_pk_add_f32 v[108:109], v[108:109], v[110:111]
	v_mov_b32_e32 v110, v107
	v_mov_b32_e32 v111, v107
	s_nop 0
	v_mov_b32_dpp v110, v108 row_bcast:15 row_mask:0xa bank_mask:0xf
	v_mov_b32_dpp v111, v109 row_bcast:15 row_mask:0xa bank_mask:0xf
	v_pk_add_f32 v[108:109], v[108:109], v[110:111]
	v_mov_b32_e32 v110, 0
	v_mov_b32_e32 v111, 0
	s_nop 0
	v_mov_b32_dpp v110, v108 row_bcast:31 row_mask:0xc bank_mask:0xf
	v_mov_b32_dpp v111, v109 row_bcast:31 row_mask:0xc bank_mask:0xf
	v_pk_add_f32 v[108:109], v[108:109], v[110:111]
	s_mov_b32 s6, 0xf800000
	s_nop 0
	v_readlane_b32 s18, v108, 63
	v_readlane_b32 s19, v109, 63
	s_nop 3
	v_mov_b32_e32 v106, s18
	v_mov_b32_e32 v107, s19
	v_mul_f32_e32 v109, 0x35800000, v106
	v_mul_f32_e32 v106, 0x35800000, v107
	v_fma_f32 v106, -v109, v109, v106
	v_add_f32_e32 v106, 0x3727c5ac, v106
	v_mul_f32_e32 v107, 0x4f800000, v106
	v_cmp_gt_f32_e32 vcc, s6, v106
	s_nop 1
	v_cndmask_b32_e32 v106, v106, v107, vcc
	v_sqrt_f32_e32 v107, v106
	s_nop 0
	v_add_u32_e32 v108, -1, v107
	v_fma_f32 v110, -v108, v107, v106
	v_cmp_ge_f32_e64 s[6:7], 0, v110
	v_add_u32_e32 v110, 1, v107
	s_nop 0
	v_cndmask_b32_e64 v108, v107, v108, s[6:7]
	v_fma_f32 v107, -v110, v107, v106
	v_cmp_lt_f32_e64 s[6:7], 0, v107
	s_nop 1
	v_cndmask_b32_e64 v107, v108, v110, s[6:7]
	v_mul_f32_e32 v108, 0x37800000, v107
	v_cndmask_b32_e32 v107, v107, v108, vcc
	v_mov_b32_e32 v108, 0x260
	v_cmp_class_f32_e32 vcc, v106, v108
	s_nop 1
	v_cndmask_b32_e32 v106, v107, v106, vcc
	v_div_scale_f32 v107, s[6:7], v106, v106, 1.0
	v_rcp_f32_e32 v108, v107
	s_movk_i32 s6, 0x360
	v_cmp_gt_u32_e64 s[6:7], s6, v0
	v_fma_f32 v110, -v107, v108, 1.0
	v_fmac_f32_e32 v108, v110, v108
	v_div_scale_f32 v110, vcc, 1.0, v106, 1.0
	v_mul_f32_e32 v111, v110, v108
	v_fma_f32 v126, -v107, v111, v110
	v_fmac_f32_e32 v111, v126, v108
	v_fma_f32 v107, -v107, v111, v110
	v_div_fmas_f32 v107, v107, v108, v111
	v_div_fixup_f32 v110, v107, v106, 1.0
	s_waitcnt vmcnt(1)
	v_mul_f32_e32 v102, v110, v102
	v_mul_f32_e32 v94, v110, v94
	s_waitcnt vmcnt(0)
	v_fma_f32 v106, -v109, v102, v98
	v_fma_f32 v98, -v109, v94, v90
	v_mul_f32_e32 v107, v110, v103
	v_mul_f32_e32 v95, v110, v95
	v_xor_b32_e32 v90, v114, v0
	v_fma_f32 v108, -v109, v107, v99
	v_fma_f32 v99, -v109, v95, v91
	v_mul_f32_e32 v103, v110, v104
	v_mul_f32_e32 v91, v110, v96
	v_mul_f32_e32 v104, v110, v105
	v_mul_f32_e32 v96, v110, v97
	v_lshlrev_b32_e32 v90, 4, v90
	v_fma_f32 v100, -v109, v103, v100
	v_fma_f32 v92, -v109, v91, v92
	v_fma_f32 v97, -v109, v104, v101
	v_fma_f32 v93, -v109, v96, v93
	v_and_b32_e32 v90, 0x70, v90
	v_fma_mixlo_f16 v101, v86, v102, v106 op_sel_hi:[1,0,0]
	v_fma_mixhi_f16 v101, v86, v107, v108 op_sel:[1,0,0] op_sel_hi:[1,0,0]
	v_pk_max_f16 v101, v101, 0
	v_fma_mixlo_f16 v86, v87, v103, v100 op_sel_hi:[1,0,0]
	v_fma_mixhi_f16 v86, v87, v104, v97 op_sel:[1,0,0] op_sel_hi:[1,0,0]
	v_pk_max_f16 v86, v86, 0
	v_fma_mixlo_f16 v87, v88, v94, v98 op_sel_hi:[1,0,0]
	v_fma_mixhi_f16 v87, v88, v95, v99 op_sel:[1,0,0] op_sel_hi:[1,0,0]
	v_pk_max_f16 v87, v87, 0
	v_fma_mixlo_f16 v88, v89, v91, v92 op_sel_hi:[1,0,0]
	v_fma_mixhi_f16 v88, v89, v96, v93 op_sel:[1,0,0] op_sel_hi:[1,0,0]
	v_pk_max_f16 v88, v88, 0
	s_and_saveexec_b64 s[8:9], s[6:7]
	s_cbranch_execz .LBB1_4
	v_or_b32_e32 v89, v125, v124
	s_movk_i32 s6, 0x80
	v_cmp_gt_u32_e32 vcc, s6, v89
	v_lshl_or_b32 v105, v114, 7, v90
	s_nop 0
	v_cndmask_b32_e32 v89, 0, v88, vcc
	v_cndmask_b32_e32 v88, 0, v87, vcc
	v_cndmask_b32_e32 v87, 0, v86, vcc
	v_cndmask_b32_e32 v86, 0, v101, vcc
	ds_write_b128 v105, v[86:89]

.LBB1_10:
	s_or_b64 exec, exec, s[8:9]
	v_lshrrev_b32_e32 v75, 4, v113
	v_and_b32_e32 v74, 15, v0
	v_lshlrev_b32_e32 v92, 7, v74
	v_bitop3_b32 v76, v0, v75, 7 bitop3:0x6c
	v_lshl_or_b32 v108, v76, 4, v92
	s_waitcnt lgkmcnt(0)
	s_barrier
	ds_read_b128 v[76:79], v108
	v_add_u32_e32 v96, 18, v74
	v_add_u32_e32 v100, 36, v74
	v_lshlrev_b32_e32 v97, 7, v96
	v_bitop3_b32 v80, v96, v75, 7 bitop3:0x6c
	v_lshlrev_b32_e32 v101, 7, v100
	v_bitop3_b32 v84, v100, v75, 7 bitop3:0x6c
	v_lshl_or_b32 v109, v80, 4, v97
	v_lshl_or_b32 v110, v84, 4, v101
	v_add_u32_e32 v104, 54, v74
	v_or_b32_e32 v113, 4, v75
	v_add_u32_e32 v118, 1, v74
	ds_read_b128 v[80:83], v109
	ds_read_b128 v[84:87], v110
	v_lshlrev_b32_e32 v105, 7, v104
	v_bitop3_b32 v88, v104, v75, 7 bitop3:0x6c
	v_bitop3_b32 v93, v0, v113, 7 bitop3:0x6c
	v_bitop3_b32 v96, v96, v113, 7 bitop3:0x6c
	v_bitop3_b32 v100, v100, v113, 7 bitop3:0x6c
	v_bitop3_b32 v104, v104, v113, 7 bitop3:0x6c
	v_lshlrev_b32_e32 v119, 7, v118
	v_bitop3_b32 v120, v118, v75, 7 bitop3:0x6c
	v_lshl_or_b32 v111, v88, 4, v105
	v_lshl_or_b32 v114, v93, 4, v92
	v_lshl_or_b32 v115, v96, 4, v97
	v_lshl_or_b32 v116, v100, 4, v101
	v_lshl_or_b32 v117, v104, 4, v105
	v_lshl_or_b32 v120, v120, 4, v119
	ds_read_b128 v[88:91], v111
	ds_read_b128 v[92:95], v114
	ds_read_b128 v[96:99], v115
	ds_read_b128 v[100:103], v116
	ds_read_b128 v[104:107], v117
	s_waitcnt lgkmcnt(7)
	v_mfma_f32_16x16x32_f16 a[0:3], v[70:73], v[76:79], 0
	ds_read_b128 v[76:79], v120
	v_add_u32_e32 v120, 19, v74
	v_lshlrev_b32_e32 v121, 7, v120
	v_bitop3_b32 v122, v120, v75, 7 bitop3:0x6c
	v_lshl_or_b32 v122, v122, 4, v121
	v_add_u32_e32 v123, 37, v74
	v_add_u32_e32 v126, 55, v74
	s_waitcnt lgkmcnt(7)
	v_mfma_f32_16x16x32_f16 a[4:7], v[70:73], v[80:83], 0
	ds_read_b128 v[80:83], v122
	v_lshlrev_b32_e32 v124, 7, v123
	v_bitop3_b32 v125, v123, v75, 7 bitop3:0x6c
	s_waitcnt lgkmcnt(7)
	v_mfma_f32_16x16x32_f16 a[8:11], v[70:73], v[84:87], 0
	v_lshlrev_b32_e32 v127, 7, v126
	v_bitop3_b32 v128, v126, v75, 7 bitop3:0x6c
	v_lshl_or_b32 v125, v125, 4, v124
	v_lshl_or_b32 v128, v128, 4, v127
	ds_read_b128 v[84:87], v125
	s_waitcnt lgkmcnt(7)
	v_mfma_f32_16x16x32_f16 a[12:15], v[70:73], v[88:91], 0
	ds_read_b128 v[70:73], v128
	v_bitop3_b32 v88, v118, v113, 7 bitop3:0x6c
	v_lshl_or_b32 v88, v88, 4, v119
	s_waitcnt lgkmcnt(7)
	v_mfma_f32_16x16x32_f16 a[0:3], v[66:69], v[92:95], a[0:3]
	v_bitop3_b32 v92, v120, v113, 7 bitop3:0x6c
	v_lshl_or_b32 v118, v92, 4, v121
	ds_read_b128 v[88:91], v88
	s_waitcnt lgkmcnt(7)
	v_mfma_f32_16x16x32_f16 a[4:7], v[66:69], v[96:99], a[4:7]
	ds_read_b128 v[92:95], v118
	v_bitop3_b32 v96, v123, v113, 7 bitop3:0x6c
	v_lshl_or_b32 v119, v96, 4, v124
	s_waitcnt lgkmcnt(7)
	v_mfma_f32_16x16x32_f16 a[8:11], v[66:69], v[100:103], a[8:11]
	v_add_u32_e32 v101, 2, v74
	v_bitop3_b32 v100, v126, v113, 7 bitop3:0x6c
	v_lshlrev_b32_e32 v102, 7, v101
	v_bitop3_b32 v103, v101, v75, 7 bitop3:0x6c
	v_lshl_or_b32 v100, v100, 4, v127
	v_lshl_or_b32 v103, v103, 4, v102
	ds_read_b128 v[96:99], v119
	s_waitcnt lgkmcnt(7)
	v_mfma_f32_16x16x32_f16 a[12:15], v[66:69], v[104:107], a[12:15]
	ds_read_b128 v[66:69], v100
	v_add_u32_e32 v106, 38, v74
	v_lshlrev_b32_e32 v107, 7, v106
	s_waitcnt lgkmcnt(7)
	v_mfma_f32_16x16x32_f16 a[0:3], v[62:65], v[76:79], a[0:3]
	ds_read_b128 v[76:79], v103
	v_add_u32_e32 v103, 20, v74
	v_lshlrev_b32_e32 v104, 7, v103
	v_bitop3_b32 v105, v103, v75, 7 bitop3:0x6c
	v_lshl_or_b32 v105, v105, 4, v104
	s_waitcnt lgkmcnt(7)
	v_mfma_f32_16x16x32_f16 a[4:7], v[62:65], v[80:83], a[4:7]
	ds_read_b128 v[80:83], v105
	s_lshl_b32 s3, s3, 7
	s_or_b32 s3, s3, 0x180
	s_waitcnt lgkmcnt(7)
	v_mfma_f32_16x16x32_f16 a[8:11], v[62:65], v[84:87], a[8:11]
	v_bitop3_b32 v84, v106, v75, 7 bitop3:0x6c
	v_lshl_or_b32 v120, v84, 4, v107
	ds_read_b128 v[84:87], v120
	s_waitcnt lgkmcnt(7)
	v_mfma_f32_16x16x32_f16 a[12:15], v[62:65], v[70:73], a[12:15]
	v_bitop3_b32 v70, v101, v113, 7 bitop3:0x6c
	ds_read_b128 v[62:65], v108 offset:7168
	v_lshl_or_b32 v70, v70, 4, v102
	s_waitcnt lgkmcnt(7)
	v_mfma_f32_16x16x32_f16 a[0:3], v[58:61], v[88:91], a[0:3]
	v_bitop3_b32 v88, v103, v113, 7 bitop3:0x6c
	ds_read_b128 v[70:73], v70
	v_lshl_or_b32 v101, v88, 4, v104
	s_waitcnt lgkmcnt(7)
	v_mfma_f32_16x16x32_f16 a[4:7], v[58:61], v[92:95], a[4:7]
	v_bitop3_b32 v92, v106, v113, 7 bitop3:0x6c
	ds_read_b128 v[88:91], v101
	s_waitcnt lgkmcnt(7)
	v_mfma_f32_16x16x32_f16 a[8:11], v[58:61], v[96:99], a[8:11]
	v_lshl_or_b32 v96, v92, 4, v107
	ds_read_b128 v[92:95], v96
	s_waitcnt lgkmcnt(7)
	v_mfma_f32_16x16x32_f16 a[12:15], v[58:61], v[66:69], a[12:15]
	ds_read_b128 v[58:61], v114 offset:7168
	s_waitcnt lgkmcnt(7)
	v_mfma_f32_16x16x32_f16 a[0:3], v[54:57], v[76:79], a[0:3]
	ds_read_b128 v[66:69], v109
	s_waitcnt lgkmcnt(7)
	v_mfma_f32_16x16x32_f16 a[4:7], v[54:57], v[80:83], a[4:7]
	ds_read_b128 v[76:79], v110
	s_waitcnt lgkmcnt(7)
	v_mfma_f32_16x16x32_f16 a[8:11], v[54:57], v[84:87], a[8:11]
	ds_read_b128 v[80:83], v111
	s_waitcnt lgkmcnt(7)
	v_mfma_f32_16x16x32_f16 a[12:15], v[54:57], v[62:65], a[12:15]
	ds_read_b128 v[54:57], v108 offset:9216
	s_waitcnt lgkmcnt(7)
	v_mfma_f32_16x16x32_f16 a[0:3], v[50:53], v[70:73], a[0:3]
	ds_read_b128 v[62:65], v115
	s_waitcnt lgkmcnt(7)
	v_mfma_f32_16x16x32_f16 a[4:7], v[50:53], v[88:91], a[4:7]
	ds_read_b128 v[70:73], v116
	s_waitcnt lgkmcnt(7)
	v_mfma_f32_16x16x32_f16 a[8:11], v[50:53], v[92:95], a[8:11]
	ds_read_b128 v[84:87], v117
	s_waitcnt lgkmcnt(7)
	v_mfma_f32_16x16x32_f16 a[12:15], v[50:53], v[58:61], a[12:15]
	ds_read_b128 v[50:53], v114 offset:9216
	s_waitcnt lgkmcnt(7)
	v_mfma_f32_16x16x32_f16 a[0:3], v[46:49], v[66:69], a[0:3]
	ds_read_b128 v[58:61], v122
	s_waitcnt lgkmcnt(7)
	v_mfma_f32_16x16x32_f16 a[4:7], v[46:49], v[76:79], a[4:7]
	ds_read_b128 v[66:69], v125
	s_waitcnt lgkmcnt(7)
	v_mfma_f32_16x16x32_f16 a[8:11], v[46:49], v[80:83], a[8:11]
	v_add_u32_e32 v80, 0x49, v74
	ds_read_b128 v[76:79], v128
	v_lshlrev_b32_e32 v81, 7, v80
	s_waitcnt lgkmcnt(7)
	v_mfma_f32_16x16x32_f16 a[12:15], v[46:49], v[54:57], a[12:15]
	v_bitop3_b32 v46, v80, v75, 7 bitop3:0x6c
	v_lshl_or_b32 v82, v46, 4, v81
	ds_read_b128 v[46:49], v82
	s_waitcnt lgkmcnt(7)
	v_mfma_f32_16x16x32_f16 a[0:3], v[42:45], v[62:65], a[0:3]
	ds_read_b128 v[54:57], v118
	s_waitcnt lgkmcnt(7)
	v_mfma_f32_16x16x32_f16 a[4:7], v[42:45], v[70:73], a[4:7]
	ds_read_b128 v[62:65], v119
	s_waitcnt lgkmcnt(7)
	v_mfma_f32_16x16x32_f16 a[8:11], v[42:45], v[84:87], a[8:11]
	ds_read_b128 v[70:73], v100
	s_waitcnt lgkmcnt(7)
	v_mfma_f32_16x16x32_f16 a[12:15], v[42:45], v[50:53], a[12:15]
	v_bitop3_b32 v42, v80, v113, 7 bitop3:0x6c
	v_lshl_or_b32 v80, v42, 4, v81
	ds_read_b128 v[42:45], v80
	s_waitcnt lgkmcnt(7)
	v_mfma_f32_16x16x32_f16 a[0:3], v[38:41], v[58:61], a[0:3]
	ds_read_b128 v[50:53], v105
	s_waitcnt lgkmcnt(7)
	v_mfma_f32_16x16x32_f16 a[4:7], v[38:41], v[66:69], a[4:7]
	ds_read_b128 v[58:61], v120
	s_waitcnt lgkmcnt(7)
	v_mfma_f32_16x16x32_f16 a[8:11], v[38:41], v[76:79], a[8:11]
	v_add_u32_e32 v76, 0x4a, v74
	ds_read_b128 v[66:69], v108 offset:7168
	v_lshlrev_b32_e32 v77, 7, v76
	s_waitcnt lgkmcnt(7)
	v_mfma_f32_16x16x32_f16 a[12:15], v[38:41], v[46:49], a[12:15]
	v_bitop3_b32 v38, v76, v75, 7 bitop3:0x6c
	v_lshl_or_b32 v78, v38, 4, v77
	ds_read_b128 v[38:41], v78
	s_waitcnt lgkmcnt(7)
	v_mfma_f32_16x16x32_f16 a[0:3], v[34:37], v[54:57], a[0:3]
	ds_read_b128 v[46:49], v101
	s_waitcnt lgkmcnt(7)
	v_mfma_f32_16x16x32_f16 a[4:7], v[34:37], v[62:65], a[4:7]
	ds_read_b128 v[54:57], v96
	s_waitcnt lgkmcnt(7)
	v_mfma_f32_16x16x32_f16 a[8:11], v[34:37], v[70:73], a[8:11]
	ds_read_b128 v[62:65], v114 offset:7168
	s_waitcnt lgkmcnt(7)
	v_mfma_f32_16x16x32_f16 a[12:15], v[34:37], v[42:45], a[12:15]
	v_bitop3_b32 v34, v76, v113, 7 bitop3:0x6c
	v_lshl_or_b32 v70, v34, 4, v77
	ds_read_b128 v[34:37], v70
	s_waitcnt lgkmcnt(7)
	v_mfma_f32_16x16x32_f16 a[0:3], v[30:33], v[50:53], a[0:3]
	ds_read_b128 v[42:45], v110
	s_waitcnt lgkmcnt(7)
	v_mfma_f32_16x16x32_f16 a[4:7], v[30:33], v[58:61], a[4:7]
	ds_read_b128 v[50:53], v111
	s_waitcnt lgkmcnt(7)
	v_mfma_f32_16x16x32_f16 a[8:11], v[30:33], v[66:69], a[8:11]
	v_add_u32_e32 v66, 0x5a, v74
	ds_read_b128 v[58:61], v108 offset:9216
	v_lshlrev_b32_e32 v67, 7, v66
	s_waitcnt lgkmcnt(7)
	v_mfma_f32_16x16x32_f16 a[12:15], v[30:33], v[38:41], a[12:15]
	v_bitop3_b32 v30, v66, v75, 7 bitop3:0x6c
	v_lshl_or_b32 v30, v30, 4, v67
	ds_read_b128 v[30:33], v30
	s_waitcnt lgkmcnt(7)
	v_mfma_f32_16x16x32_f16 a[0:3], v[26:29], v[46:49], a[0:3]
	ds_read_b128 v[38:41], v116
	s_waitcnt lgkmcnt(7)
	v_mfma_f32_16x16x32_f16 a[4:7], v[26:29], v[54:57], a[4:7]
	ds_read_b128 v[46:49], v117
	s_waitcnt lgkmcnt(7)
	v_mfma_f32_16x16x32_f16 a[8:11], v[26:29], v[62:65], a[8:11]
	ds_read_b128 v[54:57], v114 offset:9216
	s_waitcnt lgkmcnt(7)
	v_mfma_f32_16x16x32_f16 a[12:15], v[26:29], v[34:37], a[12:15]
	v_bitop3_b32 v26, v66, v113, 7 bitop3:0x6c
	v_lshl_or_b32 v26, v26, 4, v67
	ds_read_b128 v[26:29], v26
	s_waitcnt lgkmcnt(7)
	v_mfma_f32_16x16x32_f16 a[0:3], v[22:25], v[42:45], a[0:3]
	ds_read_b128 v[34:37], v125
	s_waitcnt lgkmcnt(7)
	v_mfma_f32_16x16x32_f16 a[4:7], v[22:25], v[50:53], a[4:7]
	ds_read_b128 v[42:45], v128
	s_waitcnt lgkmcnt(7)
	v_mfma_f32_16x16x32_f16 a[8:11], v[22:25], v[58:61], a[8:11]
	v_add_u32_e32 v58, 0x5b, v74
	ds_read_b128 v[50:53], v82
	v_lshlrev_b32_e32 v59, 7, v58
	s_waitcnt lgkmcnt(7)
	v_mfma_f32_16x16x32_f16 a[12:15], v[22:25], v[30:33], a[12:15]
	v_bitop3_b32 v22, v58, v75, 7 bitop3:0x6c
	v_lshl_or_b32 v22, v22, 4, v59
	ds_read_b128 v[22:25], v22
	s_waitcnt lgkmcnt(7)
	v_mfma_f32_16x16x32_f16 a[0:3], v[18:21], v[38:41], a[0:3]
	ds_read_b128 v[30:33], v119
	s_waitcnt lgkmcnt(7)
	v_mfma_f32_16x16x32_f16 a[4:7], v[18:21], v[46:49], a[4:7]
	ds_read_b128 v[38:41], v100
	s_waitcnt lgkmcnt(7)
	v_mfma_f32_16x16x32_f16 a[8:11], v[18:21], v[54:57], a[8:11]
	ds_read_b128 v[46:49], v80
	s_waitcnt lgkmcnt(7)
	v_mfma_f32_16x16x32_f16 a[12:15], v[18:21], v[26:29], a[12:15]
	v_bitop3_b32 v18, v58, v113, 7 bitop3:0x6c
	v_lshl_or_b32 v18, v18, 4, v59
	ds_read_b128 v[18:21], v18
	s_waitcnt lgkmcnt(7)
	v_mfma_f32_16x16x32_f16 a[0:3], v[14:17], v[34:37], a[0:3]
	ds_read_b128 v[26:29], v120
	s_waitcnt lgkmcnt(7)
	v_mfma_f32_16x16x32_f16 a[4:7], v[14:17], v[42:45], a[4:7]
	ds_read_b128 v[34:37], v108 offset:7168
	s_waitcnt lgkmcnt(7)
	v_mfma_f32_16x16x32_f16 a[8:11], v[14:17], v[50:53], a[8:11]
	v_add_u32_e32 v50, 0x5c, v74
	ds_read_b128 v[42:45], v78
	v_lshlrev_b32_e32 v51, 7, v50
	s_waitcnt lgkmcnt(7)
	v_mfma_f32_16x16x32_f16 a[12:15], v[14:17], v[22:25], a[12:15]
	v_bitop3_b32 v14, v50, v75, 7 bitop3:0x6c
	v_lshl_or_b32 v14, v14, 4, v51
	ds_read_b128 v[14:17], v14
	s_waitcnt lgkmcnt(7)
	v_mfma_f32_16x16x32_f16 a[0:3], v[10:13], v[30:33], a[0:3]
	ds_read_b128 v[22:25], v96
	s_waitcnt lgkmcnt(7)
	v_mfma_f32_16x16x32_f16 a[4:7], v[10:13], v[38:41], a[4:7]
	ds_read_b128 v[30:33], v114 offset:7168
	s_waitcnt lgkmcnt(7)
	v_mfma_f32_16x16x32_f16 a[8:11], v[10:13], v[46:49], a[8:11]
	ds_read_b128 v[38:41], v70
	s_waitcnt lgkmcnt(7)
	v_mfma_f32_16x16x32_f16 a[12:15], v[10:13], v[18:21], a[12:15]
	v_bitop3_b32 v10, v50, v113, 7 bitop3:0x6c
	v_lshl_or_b32 v10, v10, 4, v51
	ds_read_b128 v[10:13], v10
	s_waitcnt lgkmcnt(7)
	v_mfma_f32_16x16x32_f16 a[0:3], v[6:9], v[26:29], a[0:3]
	v_lshl_or_b32 v26, s15, 7, v74
	s_waitcnt lgkmcnt(6)
	v_mfma_f32_16x16x32_f16 a[4:7], v[6:9], v[34:37], a[4:7]
	s_waitcnt lgkmcnt(5)
	v_mfma_f32_16x16x32_f16 a[8:11], v[6:9], v[42:45], a[8:11]
	s_waitcnt lgkmcnt(4)
	v_mfma_f32_16x16x32_f16 a[12:15], v[6:9], v[14:17], a[12:15]
	s_waitcnt lgkmcnt(3)
	v_mfma_f32_16x16x32_f16 a[0:3], v[2:5], v[22:25], a[0:3]
	s_nop 7
	v_accvgpr_read_b32 v6, a0
	v_accvgpr_read_b32 v20, a1
	v_accvgpr_read_b32 v21, a2
	v_accvgpr_read_b32 v7, a3
	s_waitcnt lgkmcnt(2)
	v_mfma_f32_16x16x32_f16 a[0:3], v[2:5], v[30:33], a[4:7]
	v_mul_f32_e32 v24, v20, v20
	v_fmac_f32_e32 v24, v6, v6
	v_fmac_f32_e32 v24, v21, v21
	s_nop 4
	v_accvgpr_read_b32 v14, a2
	v_accvgpr_read_b32 v15, a3
	s_waitcnt lgkmcnt(1)
	v_mfma_f32_16x16x32_f16 a[2:5], v[2:5], v[38:41], a[8:11]
	v_accvgpr_read_b32 v8, a0
	v_accvgpr_read_b32 v9, a1
	s_nop 5
	v_accvgpr_read_b32 v18, a4
	v_accvgpr_read_b32 v19, a5
	s_waitcnt lgkmcnt(0)
	v_mfma_f32_16x16x32_f16 a[4:7], v[2:5], v[10:13], a[12:15]
	v_lshlrev_b32_e32 v2, 5, v112
	v_mov_b32_e32 v3, 0
	v_lshl_add_u64 v[12:13], s[6:7], 0, v[2:3]
	v_lshlrev_b32_e32 v2, 3, v75
	v_lshl_add_u64 v[12:13], v[12:13], 0, v[2:3]
	v_add_f32_e32 v2, 0, v6
	v_add_f32_e32 v2, v2, v20
	v_add_f32_e32 v2, v2, v21
	v_add_f32_e32 v25, v2, v7
	v_or_b32_e32 v2, s14, v26
	v_lshlrev_b64 v[22:23], 7, v[2:3]
	v_cvt_pk_f16_f32 v21, v21, v7
	v_cvt_pk_f16_f32 v20, v6, v20
	v_lshl_add_u64 v[22:23], v[12:13], 0, v[22:23]
	v_pk_mov_b32 v[6:7], v[6:7], v[8:9] op_sel:[1,0]
	global_store_dwordx2 v[22:23], v[20:21], off
	v_accvgpr_read_b32 v21, a1
	v_pk_mul_f32 v[6:7], v[6:7], v[6:7]
	v_add_f32_e32 v2, v25, v8
	v_accvgpr_read_b32 v20, a0
	v_add_f32_e32 v6, v24, v6
	v_add_f32_e32 v22, v6, v7
	v_add_f32_e32 v2, v2, v9
	v_pk_mul_f32 v[6:7], v[14:15], v[14:15]
	v_pk_mul_f32 v[20:21], v[20:21], v[20:21]
	v_add_f32_e32 v2, v2, v14
	v_add_f32_e32 v7, v22, v21
	v_add_u32_e32 v22, s14, v26
	v_add_f32_e32 v21, v2, v15
	v_add_u32_e32 v2, 0x80, v22
	v_add_f32_e32 v20, v7, v6
	v_cvt_pk_f16_f32 v6, v8, v9
	v_lshlrev_b64 v[8:9], 7, v[2:3]
	v_accvgpr_read_b32 v16, a2
	v_accvgpr_read_b32 v17, a3
	v_cvt_pk_f16_f32 v7, v14, v15
	v_lshl_add_u64 v[8:9], v[12:13], 0, v[8:9]
	global_store_dwordx2 v[8:9], v[6:7], off
	v_add_f32_e32 v2, v21, v16
	v_pk_mov_b32 v[6:7], v[14:15], v[16:17] op_sel:[1,0]
	v_accvgpr_read_b32 v9, a3
	v_pk_mul_f32 v[6:7], v[6:7], v[6:7]
	v_add_f32_e32 v2, v2, v17
	v_accvgpr_read_b32 v8, a2
	v_add_f32_e32 v6, v20, v6
	v_add_f32_e32 v2, v2, v18
	v_add_f32_e32 v14, v6, v7
	v_pk_mul_f32 v[6:7], v[18:19], v[18:19]
	v_pk_mul_f32 v[8:9], v[8:9], v[8:9]
	v_add_f32_e32 v15, v2, v19
	v_add_u32_e32 v2, 0x100, v22
	v_add_f32_e32 v7, v14, v9
	v_lshlrev_b64 v[8:9], 7, v[2:3]
	v_accvgpr_read_b32 v4, a4
	v_accvgpr_read_b32 v5, a5
	v_add_f32_e32 v14, v7, v6
	v_cvt_pk_f16_f32 v7, v18, v19
	v_cvt_pk_f16_f32 v6, v16, v17
	v_lshl_add_u64 v[8:9], v[12:13], 0, v[8:9]
	global_store_dwordx2 v[8:9], v[6:7], off
	v_pk_mov_b32 v[6:7], v[18:19], v[4:5] op_sel:[1,0]
	v_accvgpr_read_b32 v9, a5
	v_pk_mul_f32 v[6:7], v[6:7], v[6:7]
	v_add_f32_e32 v2, v15, v4
	v_accvgpr_read_b32 v8, a4
	v_add_f32_e32 v6, v14, v6
	v_accvgpr_read_b32 v10, a6
	v_accvgpr_read_b32 v11, a7
	v_add_f32_e32 v7, v6, v7
	v_add_f32_e32 v2, v2, v5
	v_pk_mul_f32 v[8:9], v[8:9], v[8:9]
	v_add_f32_e32 v6, v2, v10
	v_pk_mul_f32 v[14:15], v[10:11], v[10:11]
	v_add_f32_e32 v2, v7, v9
	v_add_f32_e32 v9, v2, v14
	v_or_b32_e32 v2, s3, v74
	v_or_b32_e32 v2, s14, v2
	v_cvt_pk_f16_f32 v14, v4, v5
	v_lshlrev_b64 v[4:5], 7, v[2:3]
	v_mul_f32_e32 v7, v11, v11
	v_cvt_pk_f16_f32 v15, v10, v11
	v_lshl_add_u64 v[4:5], v[12:13], 0, v[4:5]
	v_accvgpr_read_b32 v8, a7
	global_store_dwordx2 v[4:5], v[14:15], off
	v_pk_add_f32 v[4:5], v[6:7], v[8:9]
	v_mov_b32_e32 v2, v3
	s_nop 0
	v_mov_b32_dpp v6, v4 row_shr:1 row_mask:0xf bank_mask:0xf bound_ctrl:1
	v_mov_b32_dpp v7, v5 row_shr:1 row_mask:0xf bank_mask:0xf bound_ctrl:1
	v_pk_add_f32 v[4:5], v[4:5], v[6:7]
	s_nop 1
	v_mov_b32_dpp v6, v4 row_shr:2 row_mask:0xf bank_mask:0xf bound_ctrl:1
	v_mov_b32_dpp v7, v5 row_shr:2 row_mask:0xf bank_mask:0xf bound_ctrl:1
	v_pk_add_f32 v[4:5], v[4:5], v[6:7]
	s_nop 1
	v_mov_b32_dpp v6, v4 row_shr:4 row_mask:0xf bank_mask:0xf bound_ctrl:1
	v_mov_b32_dpp v7, v5 row_shr:4 row_mask:0xf bank_mask:0xf bound_ctrl:1
	v_pk_add_f32 v[4:5], v[4:5], v[6:7]
	s_nop 1
	v_mov_b32_dpp v6, v4 row_shr:8 row_mask:0xf bank_mask:0xf bound_ctrl:1
	v_mov_b32_dpp v7, v5 row_shr:8 row_mask:0xf bank_mask:0xf bound_ctrl:1
	v_pk_add_f32 v[4:5], v[4:5], v[6:7]
	v_mov_b32_e32 v6, v3
	v_mov_b32_e32 v7, v3
	s_nop 0
	v_mov_b32_dpp v6, v4 row_bcast:15 row_mask:0xa bank_mask:0xf
	v_mov_b32_dpp v7, v5 row_bcast:15 row_mask:0xa bank_mask:0xf
	v_pk_add_f32 v[4:5], v[4:5], v[6:7]
	s_nop 1
	v_mov_b32_dpp v2, v4 row_bcast:31 row_mask:0xc bank_mask:0xf
	v_mov_b32_dpp v3, v5 row_bcast:31 row_mask:0xc bank_mask:0xf
	s_cmp_eq_u32 s32, 0x1800
	s_cbranch_scc1 .Lkh_blockpart
	s_and_saveexec_b64 s[6:7], s[4:5]
	v_pk_add_f32 v[2:3], v[4:5], v[2:3]
	s_lshl_b32 s36, s2, 5
	v_add_u32_e32 v8, s36, v1
	global_store_dwordx2 v8, v[2:3], s[34:35]
	s_or_b64 exec, exec, s[6:7]
	s_branch .LBB1_14
.Lkh_blockpart:
	s_and_saveexec_b64 s[6:7], s[4:5]
	v_pk_add_f32 v[2:3], v[4:5], v[2:3]
	ds_write_b64 v1, v[2:3] offset:14080
	s_or_b64 exec, exec, s[6:7]
	v_cmp_eq_u32_e32 vcc, 0, v0
	s_waitcnt lgkmcnt(0)
	s_barrier
	s_and_saveexec_b64 s[4:5], vcc
	s_cbranch_execz .LBB1_14
	v_mov_b32_e32 v8, 0
	ds_read_b128 v[0:3], v8 offset:14080
	ds_read_b128 v[4:7], v8 offset:14096
	s_lshl_b32 s2, s2, 1
	s_mov_b32 s3, 0
	s_lshl_b64 s[2:3], s[2:3], 2
	s_waitcnt lgkmcnt(0)
	v_pk_add_f32 v[0:1], v[0:1], v[2:3]
	s_add_u32 s0, s22, s2
	v_pk_add_f32 v[0:1], v[0:1], v[4:5]
	s_addc_u32 s1, s23, s3
	v_pk_add_f32 v[0:1], v[0:1], v[6:7]
	global_store_dwordx2 v8, v[0:1], s[0:1]

	.amdhsa_kernel _Z4khidPKDF16_PKfS2_S2_S0_PDF16_Pf
		.amdhsa_group_segment_fixed_size 14112
		.amdhsa_private_segment_fixed_size 0
		.amdhsa_kernarg_size 56
		.amdhsa_user_sgpr_count 2
		.amdhsa_user_sgpr_dispatch_ptr 0
		.amdhsa_user_sgpr_queue_ptr 0
		.amdhsa_user_sgpr_kernarg_segment_ptr 1
		.amdhsa_user_sgpr_dispatch_id 0
		.amdhsa_user_sgpr_kernarg_preload_length 0
		.amdhsa_user_sgpr_kernarg_preload_offset 0
		.amdhsa_user_sgpr_private_segment_size 0
		.amdhsa_uses_dynamic_stack 0
		.amdhsa_enable_private_segment 0
		.amdhsa_system_sgpr_workgroup_id_x 1
		.amdhsa_system_sgpr_workgroup_id_y 0
		.amdhsa_system_sgpr_workgroup_id_z 0
		.amdhsa_system_sgpr_workgroup_info 0
		.amdhsa_system_vgpr_workitem_id 0
		.amdhsa_next_free_vgpr 184
		.amdhsa_next_free_sgpr 37
		.amdhsa_accum_offset 168
		.amdhsa_reserve_vcc 1
		.amdhsa_float_round_mode_32 0
		.amdhsa_float_round_mode_16_64 0
		.amdhsa_float_denorm_mode_32 3
		.amdhsa_float_denorm_mode_16_64 3
		.amdhsa_dx10_clamp 1
		.amdhsa_ieee_mode 1
		.amdhsa_fp16_overflow 0
		.amdhsa_tg_split 0
		.amdhsa_exception_fp_ieee_invalid_op 0
		.amdhsa_exception_fp_denorm_src 0
		.amdhsa_exception_fp_ieee_div_zero 0
		.amdhsa_exception_fp_ieee_overflow 0
		.amdhsa_exception_fp_ieee_underflow 0
		.amdhsa_exception_fp_ieee_inexact 0
		.amdhsa_exception_int_div_zero 0
	.end_amdhsa_kernel

amdhsa.kernels:
  - .agpr_count:     0
    .args:
      - .actual_access:  read_only
        .address_space:  global
        .offset:         0
        .size:           8
        .value_kind:     global_buffer
      - .actual_access:  read_only
        .address_space:  global
        .offset:         8
        .size:           8
        .value_kind:     global_buffer
      - .actual_access:  read_only
        .address_space:  global
        .offset:         16
        .size:           8
        .value_kind:     global_buffer
      - .actual_access:  read_only
        .address_space:  global
        .offset:         24
        .size:           8
        .value_kind:     global_buffer
      - .actual_access:  read_only
        .address_space:  global
        .offset:         32
        .size:           8
        .value_kind:     global_buffer
      - .actual_access:  read_only
        .address_space:  global
        .offset:         40
        .size:           8
        .value_kind:     global_buffer
      - .actual_access:  write_only
        .address_space:  global
        .offset:         48
        .size:           8
        .value_kind:     global_buffer
      - .actual_access:  write_only
        .address_space:  global
        .offset:         56
        .size:           8
        .value_kind:     global_buffer
      - .actual_access:  write_only
        .address_space:  global
        .offset:         64
        .size:           8
        .value_kind:     global_buffer
      - .actual_access:  write_only
        .address_space:  global
        .offset:         72
        .size:           8
        .value_kind:     global_buffer
    .group_segment_fixed_size: 12000
    .kernarg_segment_align: 8
    .kernarg_segment_size: 80
    .language:       OpenCL C
    .language_version:
      - 2
      - 0
    .max_flat_workgroup_size: 256
    .name:           _Z2k0PKfS0_S0_S0_S0_S0_PDF16_PfS1_S1_
    .private_segment_fixed_size: 0
    .sgpr_count:     24
    .sgpr_spill_count: 0
    .symbol:         _Z2k0PKfS0_S0_S0_S0_S0_PDF16_PfS1_S1_.kd
    .uniform_work_group_size: 1
    .uses_dynamic_stack: false
    .vgpr_count:     150
    .vgpr_spill_count: 0
    .wavefront_size: 64
  - .agpr_count:     16
    .args:
      - .actual_access:  read_only
        .address_space:  global
        .offset:         0
        .size:           8
        .value_kind:     global_buffer
      - .actual_access:  read_only
        .address_space:  global
        .offset:         8
        .size:           8
        .value_kind:     global_buffer
      - .actual_access:  read_only
        .address_space:  global
        .offset:         16
        .size:           8
        .value_kind:     global_buffer
      - .actual_access:  read_only
        .address_space:  global
        .offset:         24
        .size:           8
        .value_kind:     global_buffer
      - .actual_access:  read_only
        .address_space:  global
        .offset:         32
        .size:           8
        .value_kind:     global_buffer
      - .actual_access:  write_only
        .address_space:  global
        .offset:         40
        .size:           8
        .value_kind:     global_buffer
      - .actual_access:  write_only
        .address_space:  global
        .offset:         48
        .size:           8
        .value_kind:     global_buffer
    .group_segment_fixed_size: 14112
    .kernarg_segment_align: 8
    .kernarg_segment_size: 56
    .language:       OpenCL C
    .language_version:
      - 2
      - 0
    .max_flat_workgroup_size: 256
    .name:           _Z4khidPKDF16_PKfS2_S2_S0_PDF16_Pf
    .private_segment_fixed_size: 0
    .sgpr_count:     43
    .sgpr_spill_count: 0
    .symbol:         _Z4khidPKDF16_PKfS2_S2_S0_PDF16_Pf.kd
    .uniform_work_group_size: 1
    .uses_dynamic_stack: false
    .vgpr_count:     184
    .vgpr_spill_count: 0
    .wavefront_size: 64
  - .agpr_count:     144
    .args:
      - .actual_access:  read_only
        .address_space:  global
        .offset:         0
        .size:           8
        .value_kind:     global_buffer
      - .actual_access:  read_only
        .address_space:  global
        .offset:         8
        .size:           8
        .value_kind:     global_buffer
      - .actual_access:  read_only
        .address_space:  global
        .offset:         16
        .size:           8
        .value_kind:     global_buffer
      - .actual_access:  read_only
        .address_space:  global
        .offset:         24
        .size:           8
        .value_kind:     global_buffer
      - .address_space:  global
        .offset:         32
        .size:           8
        .value_kind:     global_buffer
      - .address_space:  global
        .offset:         40
        .size:           8
        .value_kind:     global_buffer
      - .address_space:  global
        .offset:         48
        .size:           8
        .value_kind:     global_buffer
    .group_segment_fixed_size: 0
    .kernarg_segment_align: 8
    .kernarg_segment_size: 56
    .language:       OpenCL C
    .language_version:
      - 2
      - 0
    .max_flat_workgroup_size: 256
    .name:           _Z6kfinalPKDF16_PKfS2_S2_PK15HIP_vector_typeIjLj4EES2_Pf
    .private_segment_fixed_size: 0
    .sgpr_count:     41
    .sgpr_spill_count: 0
    .symbol:         _Z6kfinalPKDF16_PKfS2_S2_PK15HIP_vector_typeIjLj4EES2_Pf.kd
    .uniform_work_group_size: 1
    .uses_dynamic_stack: false
    .vgpr_count:     400
    .vgpr_spill_count: 0
    .wavefront_size: 64
  - .agpr_count:     73
    .args:
      - .actual_access:  read_only
        .address_space:  global
        .offset:         0
        .size:           8
        .value_kind:     global_buffer
      - .actual_access:  read_only
        .address_space:  global
        .offset:         8
        .size:           8
        .value_kind:     global_buffer
      - .actual_access:  read_only
        .address_space:  global
        .offset:         16
        .size:           8
        .value_kind:     global_buffer
      - .actual_access:  read_only
        .address_space:  global
        .offset:         24
        .size:           8
        .value_kind:     global_buffer
      - .address_space:  global
        .offset:         32
        .size:           8
        .value_kind:     global_buffer
      - .address_space:  global
        .offset:         40
        .size:           8
        .value_kind:     global_buffer
      - .address_space:  global
        .offset:         48
        .size:           8
        .value_kind:     global_buffer
    .group_segment_fixed_size: 0
    .kernarg_segment_align: 8
    .kernarg_segment_size: 56
    .language:       OpenCL C
    .language_version:
      - 2
      - 0
    .max_flat_workgroup_size: 512
    .name:           _Z7kfinal3PKDF16_PKfS2_S2_PK15HIP_vector_typeIjLj4EES2_Pf
    .private_segment_fixed_size: 0
    .sgpr_count:     60
    .sgpr_spill_count: 0
    .symbol:         _Z7kfinal3PKDF16_PKfS2_S2_PK15HIP_vector_typeIjLj4EES2_Pf.kd
    .uniform_work_group_size: 1
    .uses_dynamic_stack: false
    .vgpr_count:     253
    .vgpr_spill_count: 0
    .wavefront_size: 64
